# k_fine: csorted run loads without nt (were streaming-policy loads; plain loads hit L2/MALL lines left by stageA) on top of online-softmax agg2 + stageA edits
# speedup vs baseline: 1.0458x; 1.0049x over previous
.LBB0_36:
	s_and_b64 vcc, exec, s[0:1]
	s_cbranch_vccz .LBB0_175
	v_lshrrev_b32_e32 v8, 2, v0
	v_and_b32_e32 v38, 0xf0, v8
	v_and_or_b32 v2, v0, 15, v38
	v_lshlrev_b32_e32 v4, 2, v2
	ds_read2st64_b32 v[2:3], v4 offset0:112 offset1:116
	ds_read_b32 v39, v4 offset:30720
	v_mov_b32_e32 v6, 0
	v_mov_b32_e32 v7, 0
	v_lshlrev_b32_e32 v4, 2, v1
	s_waitcnt lgkmcnt(1)
	v_readlane_b32 s0, v3, 0
	v_readlane_b32 s22, v2, 0
	s_nop 0
	v_cmp_gt_i32_e32 vcc, s0, v1
	s_and_saveexec_b64 s[0:1], vcc
	s_cbranch_execz .LBB0_39
	v_mul_u32_u24_e32 v5, 0x186c, v38
	v_lshlrev_b32_e32 v26, 2, v5
	v_mov_b32_e32 v27, 0
	v_lshl_add_u64 v[28:29], s[20:21], 0, v[26:27]
	s_ashr_i32 s23, s22, 31
	v_lshl_add_u64 v[28:29], s[22:23], 2, v[28:29]
	v_mov_b32_e32 v5, v27
	v_lshl_add_u64 v[26:27], v[28:29], 0, v[4:5]
	global_load_dword v7, v[26:27], off
.LBB0_39:
	s_or_b64 exec, exec, s[0:1]
	v_readlane_b32 s0, v3, 1
	v_readlane_b32 s22, v2, 1
	s_nop 0
	v_cmp_gt_i32_e32 vcc, s0, v1
	s_and_saveexec_b64 s[0:1], vcc
	s_cbranch_execz .LBB0_41
	v_mul_u32_u24_e32 v5, 0x186c, v38
	v_lshlrev_b32_e32 v26, 2, v5
	v_mov_b32_e32 v27, 0
	v_lshl_add_u64 v[28:29], s[20:21], 0, v[26:27]
	s_ashr_i32 s23, s22, 31
	v_lshl_add_u64 v[28:29], s[22:23], 2, v[28:29]
	v_mov_b32_e32 v5, v27
	v_lshl_add_u64 v[26:27], v[28:29], 0, v[4:5]
	v_add_co_u32_e32 v26, vcc, 0x6000, v26
	s_nop 1
	v_addc_co_u32_e32 v27, vcc, 0, v27, vcc
	global_load_dword v6, v[26:27], off offset:432
.LBB0_41:
	s_or_b64 exec, exec, s[0:1]
	v_readlane_b32 s0, v3, 2
	v_readlane_b32 s22, v2, 2
	v_mov_b32_e32 v9, 0
	v_cmp_gt_i32_e32 vcc, s0, v1
	v_mov_b32_e32 v26, 0
	s_and_saveexec_b64 s[0:1], vcc
	s_cbranch_execz .LBB0_43
	v_mul_u32_u24_e32 v5, 0x186c, v38
	v_lshlrev_b32_e32 v26, 2, v5
	v_mov_b32_e32 v27, 0
	v_lshl_add_u64 v[28:29], s[20:21], 0, v[26:27]
	s_ashr_i32 s23, s22, 31
	v_lshl_add_u64 v[28:29], s[22:23], 2, v[28:29]
	v_mov_b32_e32 v5, v27
	v_lshl_add_u64 v[26:27], v[28:29], 0, v[4:5]
	v_add_co_u32_e32 v26, vcc, 0xc000, v26
	s_nop 1
	v_addc_co_u32_e32 v27, vcc, 0, v27, vcc
	global_load_dword v26, v[26:27], off offset:864
.LBB0_43:
	s_or_b64 exec, exec, s[0:1]
	v_readlane_b32 s0, v3, 3
	v_readlane_b32 s22, v2, 3
	s_nop 0
	v_cmp_gt_i32_e32 vcc, s0, v1
	s_and_saveexec_b64 s[0:1], vcc
	s_cbranch_execz .LBB0_45
	v_mul_u32_u24_e32 v5, 0x186c, v38
	v_lshlrev_b32_e32 v28, 2, v5
	v_mov_b32_e32 v29, 0
	v_lshl_add_u64 v[40:41], s[20:21], 0, v[28:29]
	s_ashr_i32 s23, s22, 31
	v_lshl_add_u64 v[40:41], s[22:23], 2, v[40:41]
	v_mov_b32_e32 v5, v29
	v_lshl_add_u64 v[28:29], v[40:41], 0, v[4:5]
	v_add_co_u32_e32 v28, vcc, 0x12000, v28
	s_nop 1
	v_addc_co_u32_e32 v29, vcc, 0, v29, vcc
	global_load_dword v9, v[28:29], off offset:1296
.LBB0_45:
	s_or_b64 exec, exec, s[0:1]
	v_readlane_b32 s0, v3, 4
	v_readlane_b32 s22, v2, 4
	v_mov_b32_e32 v27, 0
	v_cmp_gt_i32_e32 vcc, s0, v1
	v_mov_b32_e32 v28, 0
	s_and_saveexec_b64 s[0:1], vcc
	s_cbranch_execz .LBB0_47
	v_mul_u32_u24_e32 v5, 0x186c, v38
	v_lshlrev_b32_e32 v28, 2, v5
	v_mov_b32_e32 v29, 0
	v_lshl_add_u64 v[40:41], s[20:21], 0, v[28:29]
	s_ashr_i32 s23, s22, 31
	v_lshl_add_u64 v[40:41], s[22:23], 2, v[40:41]
	v_mov_b32_e32 v5, v29
	v_lshl_add_u64 v[28:29], v[40:41], 0, v[4:5]
	v_add_co_u32_e32 v28, vcc, 0x18000, v28
	s_nop 1
	v_addc_co_u32_e32 v29, vcc, 0, v29, vcc
	global_load_dword v28, v[28:29], off offset:1728
.LBB0_47:
	s_or_b64 exec, exec, s[0:1]
	v_readlane_b32 s0, v3, 5
	v_readlane_b32 s22, v2, 5
	s_nop 0
	v_cmp_gt_i32_e32 vcc, s0, v1
	s_and_saveexec_b64 s[0:1], vcc
	s_cbranch_execz .LBB0_49
	v_mul_u32_u24_e32 v5, 0x186c, v38
	v_lshlrev_b32_e32 v40, 2, v5
	v_mov_b32_e32 v41, 0
	v_lshl_add_u64 v[42:43], s[20:21], 0, v[40:41]
	s_ashr_i32 s23, s22, 31
	v_lshl_add_u64 v[42:43], s[22:23], 2, v[42:43]
	v_mov_b32_e32 v5, v41
	v_lshl_add_u64 v[40:41], v[42:43], 0, v[4:5]
	v_add_co_u32_e32 v40, vcc, 0x1e000, v40
	s_nop 1
	v_addc_co_u32_e32 v41, vcc, 0, v41, vcc
	global_load_dword v27, v[40:41], off offset:2160
.LBB0_49:
	s_or_b64 exec, exec, s[0:1]
	v_readlane_b32 s0, v3, 6
	v_readlane_b32 s22, v2, 6
	v_mov_b32_e32 v29, 0
	v_cmp_gt_i32_e32 vcc, s0, v1
	v_mov_b32_e32 v40, 0
	s_and_saveexec_b64 s[0:1], vcc
	s_cbranch_execz .LBB0_51
	v_mul_u32_u24_e32 v5, 0x186c, v38
	v_lshlrev_b32_e32 v40, 2, v5
	v_mov_b32_e32 v41, 0
	v_lshl_add_u64 v[42:43], s[20:21], 0, v[40:41]
	s_ashr_i32 s23, s22, 31
	v_lshl_add_u64 v[42:43], s[22:23], 2, v[42:43]
	v_mov_b32_e32 v5, v41
	v_lshl_add_u64 v[40:41], v[42:43], 0, v[4:5]
	v_add_co_u32_e32 v40, vcc, 0x24000, v40
	s_nop 1
	v_addc_co_u32_e32 v41, vcc, 0, v41, vcc
	global_load_dword v40, v[40:41], off offset:2592
.LBB0_51:
	s_or_b64 exec, exec, s[0:1]
	v_readlane_b32 s0, v3, 7
	v_readlane_b32 s22, v2, 7
	s_nop 0
	v_cmp_gt_i32_e32 vcc, s0, v1
	s_and_saveexec_b64 s[0:1], vcc
	s_cbranch_execz .LBB0_53
	v_mul_u32_u24_e32 v5, 0x186c, v38
	v_lshlrev_b32_e32 v42, 2, v5
	v_mov_b32_e32 v43, 0
	v_lshl_add_u64 v[44:45], s[20:21], 0, v[42:43]
	s_ashr_i32 s23, s22, 31
	v_lshl_add_u64 v[44:45], s[22:23], 2, v[44:45]
	v_mov_b32_e32 v5, v43
	v_lshl_add_u64 v[42:43], v[44:45], 0, v[4:5]
	v_add_co_u32_e32 v42, vcc, 0x2a000, v42
	s_nop 1
	v_addc_co_u32_e32 v43, vcc, 0, v43, vcc
	global_load_dword v29, v[42:43], off offset:3024
.LBB0_53:
	s_or_b64 exec, exec, s[0:1]
	v_readlane_b32 s0, v3, 8
	v_readlane_b32 s22, v2, 8
	v_mov_b32_e32 v41, 0
	v_cmp_gt_i32_e32 vcc, s0, v1
	v_mov_b32_e32 v42, 0
	s_and_saveexec_b64 s[0:1], vcc
	s_cbranch_execz .LBB0_55
	v_mul_u32_u24_e32 v5, 0x186c, v38
	v_lshlrev_b32_e32 v42, 2, v5
	v_mov_b32_e32 v43, 0
	v_lshl_add_u64 v[44:45], s[20:21], 0, v[42:43]
	s_ashr_i32 s23, s22, 31
	v_lshl_add_u64 v[44:45], s[22:23], 2, v[44:45]
	v_mov_b32_e32 v5, v43
	v_lshl_add_u64 v[42:43], v[44:45], 0, v[4:5]
	v_add_co_u32_e32 v42, vcc, 0x30000, v42
	s_nop 1
	v_addc_co_u32_e32 v43, vcc, 0, v43, vcc
	global_load_dword v42, v[42:43], off offset:3456
.LBB0_55:
	s_or_b64 exec, exec, s[0:1]
	v_readlane_b32 s0, v3, 9
	v_readlane_b32 s22, v2, 9
	s_nop 0
	v_cmp_gt_i32_e32 vcc, s0, v1
	s_and_saveexec_b64 s[0:1], vcc
	s_cbranch_execz .LBB0_57
	v_mul_u32_u24_e32 v5, 0x186c, v38
	v_lshlrev_b32_e32 v44, 2, v5
	v_mov_b32_e32 v45, 0
	v_lshl_add_u64 v[46:47], s[20:21], 0, v[44:45]
	s_ashr_i32 s23, s22, 31
	v_lshl_add_u64 v[46:47], s[22:23], 2, v[46:47]
	v_mov_b32_e32 v5, v45
	v_lshl_add_u64 v[44:45], v[46:47], 0, v[4:5]
	v_add_co_u32_e32 v44, vcc, 0x36000, v44
	s_nop 1
	v_addc_co_u32_e32 v45, vcc, 0, v45, vcc
	global_load_dword v41, v[44:45], off offset:3888
.LBB0_57:
	s_or_b64 exec, exec, s[0:1]
	v_readlane_b32 s0, v3, 10
	v_readlane_b32 s22, v2, 10
	v_mov_b32_e32 v43, 0
	v_cmp_gt_i32_e32 vcc, s0, v1
	v_mov_b32_e32 v44, 0
	s_and_saveexec_b64 s[0:1], vcc
	s_cbranch_execz .LBB0_59
	v_mul_u32_u24_e32 v5, 0x186c, v38
	v_lshlrev_b32_e32 v44, 2, v5
	v_mov_b32_e32 v45, 0
	v_lshl_add_u64 v[46:47], s[20:21], 0, v[44:45]
	s_ashr_i32 s23, s22, 31
	v_lshl_add_u64 v[46:47], s[22:23], 2, v[46:47]
	v_mov_b32_e32 v5, v45
	v_lshl_add_u64 v[44:45], v[46:47], 0, v[4:5]
	v_add_co_u32_e32 v44, vcc, 0x3d000, v44
	s_nop 1
	v_addc_co_u32_e32 v45, vcc, 0, v45, vcc
	global_load_dword v44, v[44:45], off offset:224
.LBB0_59:
	s_or_b64 exec, exec, s[0:1]
	v_readlane_b32 s0, v3, 11
	v_readlane_b32 s22, v2, 11
	s_nop 0
	v_cmp_gt_i32_e32 vcc, s0, v1
	s_and_saveexec_b64 s[0:1], vcc
	s_cbranch_execz .LBB0_61
	v_mul_u32_u24_e32 v5, 0x186c, v38
	v_lshlrev_b32_e32 v46, 2, v5
	v_mov_b32_e32 v47, 0
	v_lshl_add_u64 v[48:49], s[20:21], 0, v[46:47]
	s_ashr_i32 s23, s22, 31
	v_lshl_add_u64 v[48:49], s[22:23], 2, v[48:49]
	v_mov_b32_e32 v5, v47
	v_lshl_add_u64 v[46:47], v[48:49], 0, v[4:5]
	v_add_co_u32_e32 v46, vcc, 0x43000, v46
	s_nop 1
	v_addc_co_u32_e32 v47, vcc, 0, v47, vcc
	global_load_dword v43, v[46:47], off offset:656
.LBB0_61:
	s_or_b64 exec, exec, s[0:1]
	v_readlane_b32 s0, v3, 12
	v_readlane_b32 s22, v2, 12
	v_mov_b32_e32 v45, 0
	v_cmp_gt_i32_e32 vcc, s0, v1
	v_mov_b32_e32 v46, 0
	s_and_saveexec_b64 s[0:1], vcc
	s_cbranch_execz .LBB0_63
	v_mul_u32_u24_e32 v5, 0x186c, v38
	v_lshlrev_b32_e32 v46, 2, v5
	v_mov_b32_e32 v47, 0
	v_lshl_add_u64 v[48:49], s[20:21], 0, v[46:47]
	s_ashr_i32 s23, s22, 31
	v_lshl_add_u64 v[48:49], s[22:23], 2, v[48:49]
	v_mov_b32_e32 v5, v47
	v_lshl_add_u64 v[46:47], v[48:49], 0, v[4:5]
	v_add_co_u32_e32 v46, vcc, 0x49000, v46
	s_nop 1
	v_addc_co_u32_e32 v47, vcc, 0, v47, vcc
	global_load_dword v46, v[46:47], off offset:1088
.LBB0_63:
	s_or_b64 exec, exec, s[0:1]
	v_readlane_b32 s0, v3, 13
	v_readlane_b32 s22, v2, 13
	s_nop 0
	v_cmp_gt_i32_e32 vcc, s0, v1
	s_and_saveexec_b64 s[0:1], vcc
	s_cbranch_execz .LBB0_65
	v_mul_u32_u24_e32 v5, 0x186c, v38
	v_lshlrev_b32_e32 v48, 2, v5
	v_mov_b32_e32 v49, 0
	v_lshl_add_u64 v[50:51], s[20:21], 0, v[48:49]
	s_ashr_i32 s23, s22, 31
	v_lshl_add_u64 v[50:51], s[22:23], 2, v[50:51]
	v_mov_b32_e32 v5, v49
	v_lshl_add_u64 v[48:49], v[50:51], 0, v[4:5]
	v_add_co_u32_e32 v48, vcc, 0x4f000, v48
	s_nop 1
	v_addc_co_u32_e32 v49, vcc, 0, v49, vcc
	global_load_dword v45, v[48:49], off offset:1520
.LBB0_65:
	s_or_b64 exec, exec, s[0:1]
	v_readlane_b32 s0, v3, 14
	v_readlane_b32 s22, v2, 14
	v_mov_b32_e32 v47, 0
	v_cmp_gt_i32_e32 vcc, s0, v1
	v_mov_b32_e32 v48, 0
	s_and_saveexec_b64 s[0:1], vcc
	s_cbranch_execz .LBB0_67
	v_mul_u32_u24_e32 v5, 0x186c, v38
	v_lshlrev_b32_e32 v48, 2, v5
	v_mov_b32_e32 v49, 0
	v_lshl_add_u64 v[50:51], s[20:21], 0, v[48:49]
	s_ashr_i32 s23, s22, 31
	v_lshl_add_u64 v[50:51], s[22:23], 2, v[50:51]
	v_mov_b32_e32 v5, v49
	v_lshl_add_u64 v[48:49], v[50:51], 0, v[4:5]
	v_add_co_u32_e32 v48, vcc, 0x55000, v48
	s_nop 1
	v_addc_co_u32_e32 v49, vcc, 0, v49, vcc
	global_load_dword v48, v[48:49], off offset:1952
.LBB0_67:
	s_or_b64 exec, exec, s[0:1]
	v_readlane_b32 s0, v3, 15
	v_readlane_b32 s22, v2, 15
	s_nop 0
	v_cmp_gt_i32_e32 vcc, s0, v1
	s_and_saveexec_b64 s[0:1], vcc
	s_cbranch_execz .LBB0_69
	v_or_b32_e32 v5, 15, v8
	v_mul_u32_u24_e32 v5, 0x186c, v5
	v_lshlrev_b32_e32 v50, 2, v5
	v_mov_b32_e32 v51, 0
	v_lshl_add_u64 v[52:53], s[20:21], 0, v[50:51]
	s_ashr_i32 s23, s22, 31
	v_lshl_add_u64 v[52:53], s[22:23], 2, v[52:53]
	v_mov_b32_e32 v5, v51
	v_lshl_add_u64 v[50:51], v[52:53], 0, v[4:5]
	global_load_dword v47, v[50:51], off
